# k3 main loop: counted vmcnt at loop head so stores stay in flight across iterations
# speedup vs baseline: 1.0414x; 1.0414x over previous
.LBB2_414:
	s_movk_i32 s0, 0xc00
	v_mov_b64_e32 v[26:27], s[42:43]
	v_mul_u32_u24_e32 v28, 0xc00, v154
	v_mad_i64_i32 v[26:27], s[0:1], v62, s0, v[26:27]
	v_or_b32_e32 v28, v28, v98
	v_mov_b32_e32 v99, 0
	v_lshl_add_u64 v[26:27], v[26:27], 0, v[98:99]
	v_or_b32_e32 v29, 0x10000, v28
	global_store_dwordx4 v[26:27], v[22:25], off
	ds_write_b128 v29, v[22:25]
	v_sub_f32_e32 v10, v10, v22
	v_or_b32_e32 v22, v101, v154
	v_sub_f32_e32 v11, v11, v23
	v_add_u32_e32 v23, v22, v102
	v_lshl_or_b32 v23, v23, 4, v103
	ds_write_b32 v23, v10
	v_add_u32_e32 v10, v22, v104
	v_lshl_or_b32 v10, v10, 4, v105
	ds_write_b32 v10, v11
	v_or_b32_e32 v10, v106, v154
	v_add_u32_e32 v10, v10, v107
	v_sub_f32_e32 v12, v12, v24
	v_lshl_or_b32 v10, v10, 4, v108
	ds_write_b32 v10, v12
	v_or_b32_e32 v10, v109, v154
	v_add_u32_e32 v10, v10, v110
	v_sub_f32_e32 v13, v13, v25
	v_lshl_or_b32 v10, v10, 4, v111
	ds_write_b32 v10, v13
	v_add_u32_e32 v10, 0x10400, v28
	ds_write_b128 v10, v[18:21]
	v_sub_f32_e32 v10, v6, v18
	v_sub_f32_e32 v11, v7, v19
	v_pk_add_f32 v[6:7], v[8:9], v[20:21] neg_lo:[0,1] neg_hi:[0,1]
	v_or_b32_e32 v8, v112, v154
	v_add_u32_e32 v9, v8, v113
	v_add_u32_e32 v8, v8, v115
	v_lshl_or_b32 v9, v9, 4, v114
	v_lshl_or_b32 v8, v8, 4, v116
	ds_write_b32 v9, v10
	ds_write_b32 v8, v11
	v_or_b32_e32 v8, v117, v154
	v_add_u32_e32 v8, v8, v118
	v_lshl_or_b32 v8, v8, 4, v119
	ds_write_b32 v8, v6
	v_or_b32_e32 v6, v120, v154
	v_add_u32_e32 v6, v6, v121
	v_lshl_or_b32 v6, v6, 4, v122
	ds_write_b32 v6, v7
	v_add_u32_e32 v6, 0x10800, v28
	ds_write_b128 v6, v[14:17]
	v_or_b32_e32 v6, v123, v154
	v_add_u32_e32 v7, v6, v124
	v_pk_add_f32 v[2:3], v[2:3], v[14:15] neg_lo:[0,1] neg_hi:[0,1]
	v_lshl_or_b32 v7, v7, 4, v125
	ds_write_b32 v7, v2
	v_add_u32_e32 v2, v6, v126
	v_lshl_or_b32 v2, v2, 4, v127
	ds_write_b32 v2, v3
	v_or_b32_e32 v2, v133, v154
	v_add_u32_e32 v2, v2, v134
	v_pk_add_f32 v[4:5], v[4:5], v[16:17] neg_lo:[0,1] neg_hi:[0,1]
	v_lshl_or_b32 v2, v2, 4, v63
	ds_write_b32 v2, v4
	v_or_b32_e32 v2, v135, v154
	v_add_u32_e32 v2, v2, v132
	v_lshl_or_b32 v2, v2, 4, v136
	v_add_lshl_u32 v4, v100, v154, 4
	s_mov_b32 s5, 0
	s_mov_b32 s4, 1.0
	ds_write_b32 v2, v5
	v_mov_b64_e32 v[2:3], s[4:5]
	v_add_u32_e32 v4, 8, v4
	s_waitcnt vmcnt(1)
	v_lshlrev_b32_e32 v40, 9, v150
	ds_write2st64_b64 v4, v[2:3], v[2:3] offset1:64
	v_or_b32_e32 v2, v40, v128
	v_lshlrev_b32_e32 v98, 4, v2
	v_lshl_add_u64 v[100:101], s[40:41], 0, v[98:99]
	s_mov_b64 s[0:1], 0x787000
	v_lshl_add_u64 v[34:35], v[100:101], 0, s[0:1]
	s_mov_b32 s0, 0x788000
	v_add_co_u32_e32 v36, vcc, s0, v100
	global_store_dwordx4 v[26:27], v[18:21], off offset:1024
	global_store_dwordx4 v[26:27], v[14:17], off offset:2048
	s_waitcnt lgkmcnt(0)
	s_barrier
	v_addc_co_u32_e32 v37, vcc, 0, v101, vcc
	global_load_dwordx4 v[2:5], v[34:35], off offset:1024
	global_load_dwordx4 v[10:13], v[34:35], off offset:2048
	global_load_dwordx4 v[14:17], v[34:35], off offset:3072
	global_load_dwordx4 v[6:9], v[36:37], off offset:-4096
	global_load_dwordx4 v[18:21], v[36:37], off
	global_load_dwordx4 v[22:25], v[36:37], off offset:1024
	global_load_dwordx4 v[26:29], v[36:37], off offset:2048
	global_load_dwordx4 v[30:33], v[36:37], off offset:3072
	v_and_b32_e32 v35, 15, v0
	v_lshrrev_b32_e32 v37, 4, v128
	v_lshlrev_b32_e32 v102, 2, v35
	v_lshlrev_b32_e32 v41, 2, v37
	v_lshlrev_b32_e32 v34, 4, v35
	v_cmp_gt_u32_e64 s[0:1], 6, v35
	v_mov_b32_e32 v35, v99
	v_or3_b32 v36, v34, v41, v40
	v_lshl_add_u64 v[104:105], s[44:45], 0, v[34:35]
	v_or_b32_e32 v34, v40, v34
	s_movk_i32 s4, 0x1000
	v_or3_b32 v153, v34, v41, s4
	v_or_b32_e32 v34, 0x11800, v98
	v_lshl_add_u64 v[118:119], s[40:41], 0, v[34:35]
	v_or_b32_e32 v34, 0x11400, v98
	v_lshl_add_u64 v[120:121], s[40:41], 0, v[34:35]
	v_or_b32_e32 v34, 0x11000, v98
	ds_read2st64_b32 v[132:133], v36 offset1:1
	v_or_b32_e32 v36, s33, v41
	v_lshl_add_u64 v[122:123], s[40:41], 0, v[34:35]
	v_or_b32_e32 v34, 0x10c00, v98
	v_or_b32_e32 v38, 1, v36
	v_lshl_add_u64 v[124:125], s[40:41], 0, v[34:35]
	v_or_b32_e32 v34, 0x10800, v98
	v_mul_u32_u24_e32 v152, 0x3000, v37
	v_ashrrev_i32_e32 v37, 31, v36
	v_ashrrev_i32_e32 v39, 31, v38
	v_lshl_add_u64 v[126:127], s[40:41], 0, v[34:35]
	v_or_b32_e32 v34, 0x10400, v98
	v_mov_b32_e32 v103, v99
	v_lshlrev_b64 v[108:109], 17, v[36:37]
	v_lshlrev_b64 v[110:111], 17, v[38:39]
	v_or_b32_e32 v38, 2, v36
	v_or_b32_e32 v36, 3, v36
	v_lshl_add_u64 v[128:129], s[40:41], 0, v[34:35]
	v_mul_u32_u24_e32 v34, 24, v150
	v_lshl_add_u64 v[106:107], s[38:39], 0, v[102:103]
	v_ashrrev_i32_e32 v39, 31, v38
	v_ashrrev_i32_e32 v37, 31, v36
	v_lshlrev_b32_e32 v103, 2, v0
	v_or_b32_e32 v98, 0x11c00, v98
	v_or_b32_e32 v34, v152, v34
	v_lshlrev_b64 v[112:113], 17, v[38:39]
	v_lshlrev_b64 v[114:115], 17, v[36:37]
	v_and_b32_e32 v116, 0x700, v103
	v_mov_b32_e32 v117, v99
	v_lshl_add_u64 v[130:131], s[40:41], 0, v[98:99]
	v_add_u32_e32 v154, v34, v102
	s_mov_b64 s[6:7], 0
	s_mov_b64 s[8:9], 0x800
	v_mov_b32_e32 v155, 0x400
	v_mov_b32_e32 v159, 0
	v_mov_b32_e32 v158, 0
	v_mov_b32_e32 v157, 0
	v_mov_b32_e32 v156, 0
	s_waitcnt vmcnt(0)
	s_branch .LBB2_417

.LBB2_417:
	s_waitcnt vmcnt(24) lgkmcnt(0)
	v_mfma_f32_16x16x4_f32 v[34:37], v132, v6, 0
	s_cmp_eq_u32 s6, 0xf0000
	v_mfma_f32_16x16x4_f32 v[38:41], v132, v8, 0
	v_mfma_f32_16x16x4_f32 v[42:45], v132, v2, 0
	v_mfma_f32_16x16x4_f32 v[46:49], v132, v4, 0
	v_mfma_f32_16x16x4_f32 v[50:53], v132, v10, 0
	v_mfma_f32_16x16x4_f32 v[54:57], v132, v12, 0
	v_mfma_f32_16x16x4_f32 v[58:61], v132, v14, 0
	v_mfma_f32_16x16x4_f32 v[62:65], v132, v16, 0
	s_waitcnt vmcnt(23)
	v_mfma_f32_16x16x4_f32 v[134:137], v132, v18, 0
	v_mfma_f32_16x16x4_f32 v[138:141], v132, v20, 0
	s_waitcnt vmcnt(22)
	v_mfma_f32_16x16x4_f32 v[142:145], v132, v22, 0
	v_mfma_f32_16x16x4_f32 v[146:149], v132, v24, 0
	s_waitcnt vmcnt(21)
	v_mfma_f32_16x16x4_f32 v[160:163], v132, v26, 0
	v_mfma_f32_16x16x4_f32 v[164:167], v132, v28, 0
	s_waitcnt vmcnt(20)
	v_mfma_f32_16x16x4_f32 v[168:171], v132, v30, 0
	v_mfma_f32_16x16x4_f32 v[172:175], v132, v32, 0
	v_mfma_f32_16x16x4_f32 v[94:97], v133, v7, v[34:37]
	v_mfma_f32_16x16x4_f32 v[90:93], v133, v9, v[38:41]
	v_mfma_f32_16x16x4_f32 v[86:89], v133, v3, v[42:45]
	v_mfma_f32_16x16x4_f32 v[82:85], v133, v5, v[46:49]
	v_mfma_f32_16x16x4_f32 v[78:81], v133, v11, v[50:53]
	v_mfma_f32_16x16x4_f32 v[74:77], v133, v13, v[54:57]
	v_mfma_f32_16x16x4_f32 v[70:73], v133, v15, v[58:61]
	v_mfma_f32_16x16x4_f32 v[66:69], v133, v17, v[62:65]
	v_mfma_f32_16x16x4_f32 v[62:65], v133, v19, v[134:137]
	v_mfma_f32_16x16x4_f32 v[58:61], v133, v21, v[138:141]
	v_mfma_f32_16x16x4_f32 v[54:57], v133, v23, v[142:145]
	v_mfma_f32_16x16x4_f32 v[50:53], v133, v25, v[146:149]
	v_mfma_f32_16x16x4_f32 v[46:49], v133, v27, v[160:163]
	v_mfma_f32_16x16x4_f32 v[42:45], v133, v29, v[164:167]
	v_mfma_f32_16x16x4_f32 v[34:37], v133, v31, v[168:171]
	v_mfma_f32_16x16x4_f32 v[38:41], v133, v33, v[172:175]
	s_cbranch_scc1 .LBB2_419
	v_lshl_add_u64 v[2:3], v[100:101], 0, s[6:7]
	v_add_co_u32_e32 v10, vcc, 0x797000, v2
	v_lshl_add_u64 v[18:19], v[122:123], 0, s[6:7]
	s_nop 0
	v_addc_co_u32_e32 v11, vcc, 0, v3, vcc
	v_lshl_add_u64 v[2:3], v[128:129], 0, s[6:7]
	v_add_co_u32_e32 v12, vcc, 0x787000, v2
	v_lshl_add_u64 v[20:21], v[120:121], 0, s[6:7]
	s_nop 0
	v_addc_co_u32_e32 v13, vcc, 0, v3, vcc
	global_load_dwordx4 v[6:9], v[10:11], off
	global_load_dwordx4 v[2:5], v[12:13], off
	v_lshl_add_u64 v[10:11], v[126:127], 0, s[6:7]
	v_add_co_u32_e32 v10, vcc, 0x787000, v10
	v_lshl_add_u64 v[12:13], v[124:125], 0, s[6:7]
	s_nop 0
	v_addc_co_u32_e32 v11, vcc, 0, v11, vcc
	v_add_co_u32_e32 v14, vcc, 0x787000, v12
	v_lshl_add_u64 v[26:27], v[118:119], 0, s[6:7]
	s_nop 0
	v_addc_co_u32_e32 v15, vcc, 0, v13, vcc
	v_add_co_u32_e32 v18, vcc, 0x787000, v18
	v_lshl_add_u64 v[28:29], v[130:131], 0, s[6:7]
	s_nop 0
	v_addc_co_u32_e32 v19, vcc, 0, v19, vcc
	v_add_co_u32_e32 v22, vcc, 0x787000, v20
	global_load_dwordx4 v[10:13], v[10:11], off
	s_nop 0
	global_load_dwordx4 v[14:17], v[14:15], off
	v_addc_co_u32_e32 v23, vcc, 0, v21, vcc
	v_add_co_u32_e32 v26, vcc, 0x787000, v26
	global_load_dwordx4 v[18:21], v[18:19], off
	s_nop 0
	global_load_dwordx4 v[22:25], v[22:23], off
	v_addc_co_u32_e32 v27, vcc, 0, v27, vcc
	v_add_co_u32_e32 v30, vcc, 0x787000, v28
	s_nop 1
	v_addc_co_u32_e32 v31, vcc, 0, v29, vcc
	global_load_dwordx4 v[26:29], v[26:27], off
	s_nop 0
	global_load_dwordx4 v[30:33], v[30:31], off
	ds_read2st64_b32 v[132:133], v153 offset1:1
.LBB2_419:
	v_max_f32_e32 v98, v90, v90
	v_max_f32_e32 v134, v94, v94
	v_max_f32_e32 v98, v134, v98
	v_max3_f32 v98, v98, v86, v82
	v_max3_f32 v98, v98, v78, v74
	v_max3_f32 v98, v98, v70, v66
	v_max3_f32 v98, v98, v62, v58
	v_max3_f32 v98, v98, v54, v50
	v_max3_f32 v98, v98, v46, v42
	v_max3_f32 v98, v98, v34, v38
	v_mov_b32_e32 v134, 0
	v_mov_b32_e32 v162, 0
	v_mov_b32_e32 v161, 0
	v_mov_b32_dpp v134, v98 row_ror:1 row_mask:0xf bank_mask:0xf
	v_max_f32_e32 v134, v134, v134
	v_max_f32_e32 v98, v98, v134
	v_mov_b32_e32 v134, 0
	v_mov_b32_e32 v166, 0
	v_mov_b32_e32 v164, 0
	v_mov_b32_dpp v134, v98 row_ror:2 row_mask:0xf bank_mask:0xf
	v_max_f32_e32 v134, v134, v134
	v_max_f32_e32 v98, v98, v134
	v_mov_b32_e32 v134, 0
	v_mov_b32_e32 v168, 0
	s_nop 0
	v_mov_b32_dpp v134, v98 row_ror:4 row_mask:0xf bank_mask:0xf
	v_max_f32_e32 v134, v134, v134
	v_max_f32_e32 v98, v98, v134
	v_mov_b32_e32 v134, 0
	s_nop 1
	v_mov_b32_dpp v134, v98 row_ror:8 row_mask:0xf bank_mask:0xf
	v_max_f32_e32 v134, v134, v134
	v_max_f32_e32 v149, v98, v134
	v_cmp_eq_f32_e32 vcc, v38, v149
	s_nop 1
	v_cndmask_b32_e64 v98, v155, 15, vcc
	v_cmp_neq_f32_e32 vcc, v34, v149
	v_sub_f32_e32 v34, v34, v149
	v_exp_f32_e32 v148, v34
	v_cndmask_b32_e32 v98, 14, v98, vcc
	v_cmp_neq_f32_e32 vcc, v42, v149
	v_sub_f32_e32 v42, v42, v149
	v_exp_f32_e32 v147, v42
	v_cndmask_b32_e32 v98, 13, v98, vcc
	v_cmp_neq_f32_e32 vcc, v46, v149
	v_sub_f32_e32 v46, v46, v149
	v_exp_f32_e32 v146, v46
	v_cndmask_b32_e32 v98, 12, v98, vcc
	v_cmp_neq_f32_e32 vcc, v50, v149
	v_sub_f32_e32 v50, v50, v149
	v_exp_f32_e32 v145, v50
	v_cndmask_b32_e32 v98, 11, v98, vcc
	v_cmp_neq_f32_e32 vcc, v54, v149
	v_sub_f32_e32 v54, v54, v149
	v_exp_f32_e32 v144, v54
	v_cndmask_b32_e32 v98, 10, v98, vcc
	v_cmp_neq_f32_e32 vcc, v58, v149
	v_sub_f32_e32 v58, v58, v149
	v_exp_f32_e32 v143, v58
	v_cndmask_b32_e32 v98, 9, v98, vcc
	v_cmp_neq_f32_e32 vcc, v62, v149
	v_sub_f32_e32 v62, v62, v149
	v_exp_f32_e32 v142, v62
	v_cndmask_b32_e32 v98, 8, v98, vcc
	v_cmp_neq_f32_e32 vcc, v66, v149
	v_sub_f32_e32 v66, v66, v149
	v_exp_f32_e32 v141, v66
	v_cndmask_b32_e32 v98, 7, v98, vcc
	v_cmp_neq_f32_e32 vcc, v70, v149
	v_sub_f32_e32 v70, v70, v149
	v_exp_f32_e32 v140, v70
	v_cndmask_b32_e32 v98, 6, v98, vcc
	v_cmp_neq_f32_e32 vcc, v74, v149
	v_sub_f32_e32 v74, v74, v149
	v_exp_f32_e32 v139, v74
	v_cndmask_b32_e32 v98, 5, v98, vcc
	v_cmp_neq_f32_e32 vcc, v78, v149
	v_sub_f32_e32 v78, v78, v149
	v_exp_f32_e32 v138, v78
	v_cndmask_b32_e32 v98, 4, v98, vcc
	v_cmp_neq_f32_e32 vcc, v82, v149
	v_sub_f32_e32 v82, v82, v149
	v_exp_f32_e32 v137, v82
	v_cndmask_b32_e32 v98, 3, v98, vcc
	v_cmp_neq_f32_e32 vcc, v86, v149
	v_sub_f32_e32 v86, v86, v149
	v_exp_f32_e32 v136, v86
	v_cndmask_b32_e32 v98, 2, v98, vcc
	v_cmp_neq_f32_e32 vcc, v90, v149
	v_sub_f32_e32 v90, v90, v149
	v_sub_f32_e32 v34, v38, v149
	v_cndmask_b32_e32 v98, 1, v98, vcc
	v_cmp_neq_f32_e32 vcc, v94, v149
	v_sub_f32_e32 v94, v94, v149
	v_exp_f32_e32 v149, v34
	v_cndmask_b32_e32 v98, 0, v98, vcc
	v_lshlrev_b32_e32 v134, 4, v98
	v_and_b32_e32 v134, 0x7fffffc0, v134
	v_and_b32_e32 v135, 3, v98
	v_or3_b32 v134, v135, v134, v102
	v_cmp_gt_u32_e32 vcc, 16, v98
	v_exp_f32_e32 v135, v90
	v_max_f32_e32 v38, v95, v95
	v_cndmask_b32_e32 v98, v155, v134, vcc
	v_exp_f32_e32 v134, v94
	s_nop 0
	v_min_i32_dpp v98, v98, v98 row_ror:1 row_mask:0xf bank_mask:0xf bound_ctrl:1
	v_add_f32_e32 v82, 0, v134
	v_add_f32_e32 v82, v82, v135
	v_add_f32_e32 v82, v82, v136
	v_add_f32_e32 v82, v82, v137
	v_add_f32_e32 v66, v82, v138
	v_add_f32_e32 v66, v66, v139
	v_add_f32_e32 v66, v66, v140
	v_add_f32_e32 v66, v66, v141
	v_add_f32_e32 v50, v66, v142
	v_add_f32_e32 v50, v50, v143
	v_add_f32_e32 v50, v50, v144
	v_add_f32_e32 v50, v50, v145
	v_add_f32_e32 v34, v50, v146
	v_add_f32_e32 v34, v34, v147
	v_add_f32_e32 v34, v34, v148
	v_add_f32_e32 v34, v34, v149
	v_min_i32_dpp v98, v98, v98 row_ror:2 row_mask:0xf bank_mask:0xf bound_ctrl:1
	s_nop 0
	v_add_f32_dpp v34, v34, v34 row_ror:1 row_mask:0xf bank_mask:0xf bound_ctrl:1
	v_min_i32_dpp v98, v98, v98 row_ror:4 row_mask:0xf bank_mask:0xf bound_ctrl:1
	s_nop 0
	v_add_f32_dpp v34, v34, v34 row_ror:2 row_mask:0xf bank_mask:0xf bound_ctrl:1
	v_mov_b32_dpp v162, v98 row_ror:8 row_mask:0xf bank_mask:0xf
	s_nop 0
	v_add_f32_dpp v160, v34, v34 row_ror:4 row_mask:0xf bank_mask:0xf bound_ctrl:1
	v_max_f32_e32 v34, v91, v91
	v_max_f32_e32 v34, v38, v34
	v_max3_f32 v34, v34, v87, v83
	v_max3_f32 v34, v34, v79, v75
	v_max3_f32 v34, v34, v71, v67
	v_max3_f32 v34, v34, v63, v59
	v_max3_f32 v34, v34, v55, v51
	v_max3_f32 v34, v34, v47, v43
	v_max3_f32 v34, v34, v35, v39
	v_mov_b32_e32 v38, 0
	v_mov_b32_dpp v161, v160 row_ror:8 row_mask:0xf bank_mask:0xf
	s_nop 0
	v_mov_b32_dpp v38, v34 row_ror:1 row_mask:0xf bank_mask:0xf
	v_max_f32_e32 v38, v38, v38
	v_max_f32_e32 v34, v34, v38
	v_mov_b32_e32 v38, 0
	s_nop 1
	v_mov_b32_dpp v38, v34 row_ror:2 row_mask:0xf bank_mask:0xf
	v_max_f32_e32 v38, v38, v38
	v_max_f32_e32 v34, v34, v38
	v_mov_b32_e32 v38, 0
	s_nop 1
	v_mov_b32_dpp v38, v34 row_ror:4 row_mask:0xf bank_mask:0xf
	v_max_f32_e32 v38, v38, v38
	v_max_f32_e32 v34, v34, v38
	v_mov_b32_e32 v38, 0
	s_nop 1
	v_mov_b32_dpp v38, v34 row_ror:8 row_mask:0xf bank_mask:0xf
	v_max_f32_e32 v38, v38, v38
	v_max_f32_e32 v38, v34, v38
	v_cmp_eq_f32_e32 vcc, v39, v38
	s_nop 1
	v_cndmask_b32_e64 v34, v155, 15, vcc
	v_cmp_neq_f32_e32 vcc, v35, v38
	s_nop 1
	v_cndmask_b32_e32 v34, 14, v34, vcc
	v_cmp_neq_f32_e32 vcc, v43, v38
	s_nop 1
	v_cndmask_b32_e32 v34, 13, v34, vcc
	v_cmp_neq_f32_e32 vcc, v47, v38
	s_nop 1
	v_cndmask_b32_e32 v34, 12, v34, vcc
	v_cmp_neq_f32_e32 vcc, v51, v38
	s_nop 1
	v_cndmask_b32_e32 v34, 11, v34, vcc
	v_cmp_neq_f32_e32 vcc, v55, v38
	s_nop 1
	v_cndmask_b32_e32 v34, 10, v34, vcc
	v_cmp_neq_f32_e32 vcc, v59, v38
	s_nop 1
	v_cndmask_b32_e32 v34, 9, v34, vcc
	v_cmp_neq_f32_e32 vcc, v63, v38
	s_nop 1
	v_cndmask_b32_e32 v34, 8, v34, vcc
	v_cmp_neq_f32_e32 vcc, v67, v38
	s_nop 1
	v_cndmask_b32_e32 v34, 7, v34, vcc
	v_cmp_neq_f32_e32 vcc, v71, v38
	s_nop 1
	v_cndmask_b32_e32 v34, 6, v34, vcc
	v_cmp_neq_f32_e32 vcc, v75, v38
	s_nop 1
	v_cndmask_b32_e32 v34, 5, v34, vcc
	v_cmp_neq_f32_e32 vcc, v79, v38
	s_nop 1
	v_cndmask_b32_e32 v34, 4, v34, vcc
	v_cmp_neq_f32_e32 vcc, v83, v38
	s_nop 1
	v_cndmask_b32_e32 v34, 3, v34, vcc
	v_cmp_neq_f32_e32 vcc, v87, v38
	s_nop 1
	v_cndmask_b32_e32 v34, 2, v34, vcc
	v_cmp_neq_f32_e32 vcc, v91, v38
	s_nop 1
	v_cndmask_b32_e32 v34, 1, v34, vcc
	v_cmp_neq_f32_e32 vcc, v95, v38
	s_nop 1
	v_cndmask_b32_e32 v34, 0, v34, vcc
	v_lshlrev_b32_e32 v42, 4, v34
	v_and_b32_e32 v42, 0x7fffffc0, v42
	v_and_b32_e32 v46, 3, v34
	v_or3_b32 v42, v46, v42, v102
	v_cmp_gt_u32_e32 vcc, 16, v34
	s_nop 1
	v_cndmask_b32_e32 v34, v155, v42, vcc
	v_sub_f32_e32 v42, v79, v38
	v_exp_f32_e32 v74, v42
	v_min_i32_dpp v34, v34, v34 row_ror:1 row_mask:0xf bank_mask:0xf bound_ctrl:1
	v_sub_f32_e32 v42, v75, v38
	v_exp_f32_e32 v75, v42
	v_min_i32_dpp v34, v34, v34 row_ror:2 row_mask:0xf bank_mask:0xf bound_ctrl:1
	v_sub_f32_e32 v42, v71, v38
	v_exp_f32_e32 v66, v42
	v_min_i32_dpp v165, v34, v34 row_ror:4 row_mask:0xf bank_mask:0xf bound_ctrl:1
	v_sub_f32_e32 v34, v95, v38
	v_exp_f32_e32 v90, v34
	v_sub_f32_e32 v34, v91, v38
	v_exp_f32_e32 v91, v34
	v_sub_f32_e32 v34, v87, v38
	v_exp_f32_e32 v82, v34
	v_sub_f32_e32 v34, v83, v38
	v_exp_f32_e32 v83, v34
	v_add_f32_e32 v34, 0, v90
	v_add_f32_e32 v34, v34, v91
	v_add_f32_e32 v34, v34, v82
	v_sub_f32_e32 v42, v67, v38
	v_add_f32_e32 v34, v34, v83
	v_exp_f32_e32 v67, v42
	v_sub_f32_e32 v42, v63, v38
	v_add_f32_e32 v34, v34, v74
	v_exp_f32_e32 v58, v42
	v_sub_f32_e32 v42, v59, v38
	v_add_f32_e32 v34, v34, v75
	v_exp_f32_e32 v59, v42
	v_sub_f32_e32 v42, v55, v38
	v_add_f32_e32 v34, v34, v66
	v_exp_f32_e32 v50, v42
	v_sub_f32_e32 v42, v51, v38
	v_add_f32_e32 v34, v34, v67
	v_exp_f32_e32 v51, v42
	v_add_f32_e32 v34, v34, v58
	v_add_f32_e32 v34, v34, v59
	v_add_f32_e32 v34, v34, v50
	v_add_f32_e32 v46, v34, v51
	v_sub_f32_e32 v34, v47, v38
	v_exp_f32_e32 v42, v34
	v_sub_f32_e32 v34, v43, v38
	v_exp_f32_e32 v43, v34
	v_sub_f32_e32 v34, v35, v38
	v_exp_f32_e32 v34, v34
	v_sub_f32_e32 v35, v39, v38
	v_exp_f32_e32 v35, v35
	v_add_f32_e32 v38, v46, v42
	v_add_f32_e32 v38, v38, v43
	v_add_f32_e32 v38, v38, v34
	v_add_f32_e32 v38, v38, v35
	v_max_f32_e32 v39, v96, v96
	v_mov_b32_dpp v166, v165 row_ror:8 row_mask:0xf bank_mask:0xf
	v_add_f32_dpp v38, v38, v38 row_ror:1 row_mask:0xf bank_mask:0xf bound_ctrl:1
	s_nop 1
	v_add_f32_dpp v38, v38, v38 row_ror:2 row_mask:0xf bank_mask:0xf bound_ctrl:1
	s_nop 1
	v_add_f32_dpp v163, v38, v38 row_ror:4 row_mask:0xf bank_mask:0xf bound_ctrl:1
	v_max_f32_e32 v38, v92, v92
	v_max_f32_e32 v38, v39, v38
	v_max3_f32 v38, v38, v88, v84
	v_max3_f32 v38, v38, v80, v76
	v_max3_f32 v38, v38, v72, v68
	v_max3_f32 v38, v38, v64, v60
	v_max3_f32 v38, v38, v56, v52
	v_max3_f32 v38, v38, v48, v44
	v_max3_f32 v38, v38, v36, v40
	v_mov_b32_e32 v39, 0
	v_mov_b32_dpp v164, v163 row_ror:8 row_mask:0xf bank_mask:0xf
	s_nop 0
	v_mov_b32_dpp v39, v38 row_ror:1 row_mask:0xf bank_mask:0xf
	v_max_f32_e32 v39, v39, v39
	v_max_f32_e32 v38, v38, v39
	v_mov_b32_e32 v39, 0
	s_nop 1
	v_mov_b32_dpp v39, v38 row_ror:2 row_mask:0xf bank_mask:0xf
	v_max_f32_e32 v39, v39, v39
	v_max_f32_e32 v38, v38, v39
	v_mov_b32_e32 v39, 0
	s_nop 1
	v_mov_b32_dpp v39, v38 row_ror:4 row_mask:0xf bank_mask:0xf
	v_max_f32_e32 v39, v39, v39
	v_max_f32_e32 v38, v38, v39
	v_mov_b32_e32 v39, 0
	s_nop 1
	v_mov_b32_dpp v39, v38 row_ror:8 row_mask:0xf bank_mask:0xf
	v_max_f32_e32 v39, v39, v39
	v_max_f32_e32 v95, v38, v39
	v_cmp_eq_f32_e32 vcc, v40, v95
	v_sub_f32_e32 v47, v84, v95
	v_exp_f32_e32 v47, v47
	v_cndmask_b32_e64 v38, v155, 15, vcc
	v_cmp_neq_f32_e32 vcc, v36, v95
	v_sub_f32_e32 v55, v76, v95
	v_exp_f32_e32 v55, v55
	v_cndmask_b32_e32 v38, 14, v38, vcc
	v_cmp_neq_f32_e32 vcc, v44, v95
	v_sub_f32_e32 v62, v72, v95
	v_exp_f32_e32 v62, v62
	v_cndmask_b32_e32 v38, 13, v38, vcc
	v_cmp_neq_f32_e32 vcc, v48, v95
	v_sub_f32_e32 v63, v68, v95
	v_exp_f32_e32 v63, v63
	v_cndmask_b32_e32 v38, 12, v38, vcc
	v_cmp_neq_f32_e32 vcc, v52, v95
	v_sub_f32_e32 v52, v52, v95
	v_exp_f32_e32 v79, v52
	v_cndmask_b32_e32 v38, 11, v38, vcc
	v_cmp_neq_f32_e32 vcc, v56, v95
	v_sub_f32_e32 v56, v56, v95
	v_exp_f32_e32 v78, v56
	v_cndmask_b32_e32 v38, 10, v38, vcc
	v_cmp_neq_f32_e32 vcc, v60, v95
	v_sub_f32_e32 v60, v60, v95
	v_exp_f32_e32 v71, v60
	v_cndmask_b32_e32 v38, 9, v38, vcc
	v_cmp_neq_f32_e32 vcc, v64, v95
	v_sub_f32_e32 v64, v64, v95
	v_sub_f32_e32 v48, v48, v95
	v_cndmask_b32_e32 v38, 8, v38, vcc
	v_cmp_neq_f32_e32 vcc, v68, v95
	v_exp_f32_e32 v86, v48
	v_sub_f32_e32 v44, v44, v95
	v_cndmask_b32_e32 v38, 7, v38, vcc
	v_cmp_neq_f32_e32 vcc, v72, v95
	v_exp_f32_e32 v87, v44
	v_sub_f32_e32 v36, v36, v95
	v_cndmask_b32_e32 v38, 6, v38, vcc
	v_cmp_neq_f32_e32 vcc, v76, v95
	v_exp_f32_e32 v94, v36
	v_sub_f32_e32 v36, v40, v95
	v_cndmask_b32_e32 v38, 5, v38, vcc
	v_cmp_neq_f32_e32 vcc, v80, v95
	v_max_f32_e32 v40, v97, v97
	v_mov_b32_e32 v56, 0
	v_cndmask_b32_e32 v38, 4, v38, vcc
	v_cmp_neq_f32_e32 vcc, v84, v95
	v_mov_b32_e32 v72, 0
	s_nop 0
	v_cndmask_b32_e32 v38, 3, v38, vcc
	v_cmp_neq_f32_e32 vcc, v88, v95
	s_nop 1
	v_cndmask_b32_e32 v38, 2, v38, vcc
	v_cmp_neq_f32_e32 vcc, v92, v95
	s_nop 1
	v_cndmask_b32_e32 v38, 1, v38, vcc
	v_cmp_neq_f32_e32 vcc, v96, v95
	s_nop 1
	v_cndmask_b32_e32 v38, 0, v38, vcc
	v_lshlrev_b32_e32 v39, 4, v38
	v_and_b32_e32 v39, 0x7fffffc0, v39
	v_and_b32_e32 v46, 3, v38
	v_or3_b32 v39, v46, v39, v102
	v_cmp_gt_u32_e32 vcc, 16, v38
	v_sub_f32_e32 v46, v88, v95
	v_exp_f32_e32 v46, v46
	v_cndmask_b32_e32 v38, v155, v39, vcc
	v_sub_f32_e32 v39, v92, v95
	v_exp_f32_e32 v39, v39
	v_min_i32_dpp v38, v38, v38 row_ror:1 row_mask:0xf bank_mask:0xf bound_ctrl:1
	s_nop 1
	v_min_i32_dpp v38, v38, v38 row_ror:2 row_mask:0xf bank_mask:0xf bound_ctrl:1
	s_nop 1
	v_min_i32_dpp v167, v38, v38 row_ror:4 row_mask:0xf bank_mask:0xf bound_ctrl:1
	v_sub_f32_e32 v38, v96, v95
	v_exp_f32_e32 v38, v38
	v_mov_b32_dpp v168, v167 row_ror:8 row_mask:0xf bank_mask:0xf
	v_add_f32_e32 v54, 0, v38
	v_add_f32_e32 v54, v54, v39
	v_add_f32_e32 v54, v54, v46
	v_add_f32_e32 v70, v54, v47
	v_sub_f32_e32 v54, v80, v95
	v_exp_f32_e32 v54, v54
	v_exp_f32_e32 v95, v36
	v_add_f32_e32 v68, v70, v54
	v_exp_f32_e32 v70, v64
	v_add_f32_e32 v68, v68, v55
	v_add_f32_e32 v68, v68, v62
	v_add_f32_e32 v68, v68, v63
	v_add_f32_e32 v52, v68, v70
	v_add_f32_e32 v52, v52, v71
	v_add_f32_e32 v52, v52, v78
	v_add_f32_e32 v52, v52, v79
	v_add_f32_e32 v36, v52, v86
	v_add_f32_e32 v36, v36, v87
	v_add_f32_e32 v36, v36, v94
	v_add_f32_e32 v36, v36, v95
	s_nop 1
	v_add_f32_dpp v36, v36, v36 row_ror:1 row_mask:0xf bank_mask:0xf bound_ctrl:1
	s_nop 1
	v_add_f32_dpp v36, v36, v36 row_ror:2 row_mask:0xf bank_mask:0xf bound_ctrl:1
	s_nop 1
	v_add_f32_dpp v48, v36, v36 row_ror:4 row_mask:0xf bank_mask:0xf bound_ctrl:1
	v_max_f32_e32 v36, v93, v93
	v_max_f32_e32 v36, v40, v36
	v_max3_f32 v36, v36, v89, v85
	v_max3_f32 v36, v36, v81, v77
	v_max3_f32 v36, v36, v73, v69
	v_max3_f32 v36, v36, v65, v61
	v_max3_f32 v36, v36, v57, v53
	v_max3_f32 v36, v36, v49, v45
	v_max3_f32 v36, v36, v37, v41
	v_mov_b32_e32 v40, 0
	v_mov_b32_dpp v56, v48 row_ror:8 row_mask:0xf bank_mask:0xf
	s_nop 0
	v_mov_b32_dpp v40, v36 row_ror:1 row_mask:0xf bank_mask:0xf
	v_max_f32_e32 v40, v40, v40
	v_max_f32_e32 v36, v36, v40
	v_mov_b32_e32 v40, 0
	s_nop 1
	v_mov_b32_dpp v40, v36 row_ror:2 row_mask:0xf bank_mask:0xf
	v_max_f32_e32 v40, v40, v40
	v_max_f32_e32 v36, v36, v40
	v_mov_b32_e32 v40, 0
	s_nop 1
	v_mov_b32_dpp v40, v36 row_ror:4 row_mask:0xf bank_mask:0xf
	v_max_f32_e32 v40, v40, v40
	v_max_f32_e32 v36, v36, v40
	v_mov_b32_e32 v40, 0
	s_nop 1
	v_mov_b32_dpp v40, v36 row_ror:8 row_mask:0xf bank_mask:0xf
	v_max_f32_e32 v40, v40, v40
	v_max_f32_e32 v40, v36, v40
	v_cmp_eq_f32_e32 vcc, v41, v40
	s_nop 1
	v_cndmask_b32_e64 v36, v155, 15, vcc
	v_cmp_neq_f32_e32 vcc, v37, v40
	s_nop 1
	v_cndmask_b32_e32 v36, 14, v36, vcc
	v_cmp_neq_f32_e32 vcc, v45, v40
	s_nop 1
	v_cndmask_b32_e32 v36, 13, v36, vcc
	v_cmp_neq_f32_e32 vcc, v49, v40
	s_nop 1
	v_cndmask_b32_e32 v36, 12, v36, vcc
	v_cmp_neq_f32_e32 vcc, v53, v40
	s_nop 1
	v_cndmask_b32_e32 v36, 11, v36, vcc
	v_cmp_neq_f32_e32 vcc, v57, v40
	s_nop 1
	v_cndmask_b32_e32 v36, 10, v36, vcc
	v_cmp_neq_f32_e32 vcc, v61, v40
	s_nop 1
	v_cndmask_b32_e32 v36, 9, v36, vcc
	v_cmp_neq_f32_e32 vcc, v65, v40
	s_nop 1
	v_cndmask_b32_e32 v36, 8, v36, vcc
	v_cmp_neq_f32_e32 vcc, v69, v40
	s_nop 1
	v_cndmask_b32_e32 v36, 7, v36, vcc
	v_cmp_neq_f32_e32 vcc, v73, v40
	s_nop 1
	v_cndmask_b32_e32 v36, 6, v36, vcc
	v_cmp_neq_f32_e32 vcc, v77, v40
	s_nop 1
	v_cndmask_b32_e32 v36, 5, v36, vcc
	v_cmp_neq_f32_e32 vcc, v81, v40
	s_nop 1
	v_cndmask_b32_e32 v36, 4, v36, vcc
	v_cmp_neq_f32_e32 vcc, v85, v40
	s_nop 1
	v_cndmask_b32_e32 v36, 3, v36, vcc
	v_cmp_neq_f32_e32 vcc, v89, v40
	s_nop 1
	v_cndmask_b32_e32 v36, 2, v36, vcc
	v_cmp_neq_f32_e32 vcc, v93, v40
	s_nop 1
	v_cndmask_b32_e32 v36, 1, v36, vcc
	v_cmp_neq_f32_e32 vcc, v97, v40
	s_nop 1
	v_cndmask_b32_e32 v36, 0, v36, vcc
	v_lshlrev_b32_e32 v44, 4, v36
	v_and_b32_e32 v44, 0x7fffffc0, v44
	v_and_b32_e32 v52, 3, v36
	v_or3_b32 v44, v52, v44, v102
	v_cmp_gt_u32_e32 vcc, 16, v36
	s_nop 1
	v_cndmask_b32_e32 v36, v155, v44, vcc
	v_sub_f32_e32 v44, v81, v40
	v_exp_f32_e32 v76, v44
	v_min_i32_dpp v36, v36, v36 row_ror:1 row_mask:0xf bank_mask:0xf bound_ctrl:1
	v_sub_f32_e32 v44, v77, v40
	v_exp_f32_e32 v77, v44
	v_min_i32_dpp v36, v36, v36 row_ror:2 row_mask:0xf bank_mask:0xf bound_ctrl:1
	v_sub_f32_e32 v44, v73, v40
	v_exp_f32_e32 v68, v44
	v_min_i32_dpp v64, v36, v36 row_ror:4 row_mask:0xf bank_mask:0xf bound_ctrl:1
	v_sub_f32_e32 v36, v97, v40
	v_exp_f32_e32 v92, v36
	v_sub_f32_e32 v36, v93, v40
	v_exp_f32_e32 v93, v36
	v_sub_f32_e32 v36, v89, v40
	v_exp_f32_e32 v84, v36
	v_sub_f32_e32 v36, v85, v40
	v_exp_f32_e32 v85, v36
	v_add_f32_e32 v36, 0, v92
	v_add_f32_e32 v36, v36, v93
	v_add_f32_e32 v36, v36, v84
	v_sub_f32_e32 v44, v69, v40
	v_add_f32_e32 v36, v36, v85
	v_exp_f32_e32 v69, v44
	v_sub_f32_e32 v44, v65, v40
	v_add_f32_e32 v36, v36, v76
	v_exp_f32_e32 v60, v44
	v_sub_f32_e32 v44, v61, v40
	v_add_f32_e32 v36, v36, v77
	v_exp_f32_e32 v61, v44
	v_sub_f32_e32 v44, v57, v40
	v_add_f32_e32 v36, v36, v68
	v_exp_f32_e32 v52, v44
	v_sub_f32_e32 v44, v53, v40
	v_add_f32_e32 v36, v36, v69
	v_exp_f32_e32 v53, v44
	v_add_f32_e32 v36, v36, v60
	v_add_f32_e32 v36, v36, v61
	v_add_f32_e32 v36, v36, v52
	v_add_f32_e32 v57, v36, v53
	v_sub_f32_e32 v36, v49, v40
	v_exp_f32_e32 v44, v36
	v_sub_f32_e32 v36, v45, v40
	v_exp_f32_e32 v45, v36
	v_sub_f32_e32 v36, v37, v40
	v_exp_f32_e32 v36, v36
	v_sub_f32_e32 v37, v41, v40
	v_exp_f32_e32 v37, v37
	v_add_f32_e32 v40, v57, v44
	v_add_f32_e32 v40, v40, v45
	v_add_f32_e32 v40, v40, v36
	v_add_f32_e32 v40, v40, v37
	v_mov_b32_e32 v57, 0
	v_mov_b32_dpp v72, v64 row_ror:8 row_mask:0xf bank_mask:0xf
	v_add_f32_dpp v40, v40, v40 row_ror:1 row_mask:0xf bank_mask:0xf bound_ctrl:1
	s_nop 1
	v_add_f32_dpp v40, v40, v40 row_ror:2 row_mask:0xf bank_mask:0xf bound_ctrl:1
	s_nop 1
	v_add_f32_dpp v49, v40, v40 row_ror:4 row_mask:0xf bank_mask:0xf bound_ctrl:1
	v_mov_b64_e32 v[40:41], v[116:117]
	s_nop 0
	v_mov_b32_dpp v57, v49 row_ror:8 row_mask:0xf bank_mask:0xf
	s_and_saveexec_b64 s[10:11], s[0:1]
	s_cbranch_execz .LBB2_416
	s_cmp_eq_u32 s6, 0
	s_cbranch_scc1 .LBB2_415
	ds_read_b32 v40, v154 offset:65344
	v_add_u32_e32 v41, 0x10b40, v154
	v_add_u32_e32 v65, 0x11740, v154
	v_add_u32_e32 v73, 0x12340, v154
	ds_read_b32 v80, v41
	ds_read_b32 v81, v65
	ds_read_b32 v88, v73
	s_cmp_eq_u32 s6, 0xf0000
	s_cbranch_scc1 .Lk3_pend_last
	s_waitcnt vmcnt(24)
	s_branch .Lk3_pend_ready
.Lk3_pend_last:
	s_waitcnt vmcnt(16)
.Lk3_pend_ready:
	s_waitcnt lgkmcnt(3)
	v_add_f32_e32 v40, v159, v40
	ds_write_b32 v154, v40 offset:65344
	s_waitcnt lgkmcnt(3)
	v_add_f32_e32 v40, v158, v80
	ds_write_b32 v41, v40
	s_waitcnt lgkmcnt(3)
	v_add_f32_e32 v40, v157, v81
	ds_write_b32 v65, v40
	s_waitcnt lgkmcnt(3)
	v_add_f32_e32 v40, v156, v88
	ds_write_b32 v73, v40
	s_branch .LBB2_415
